# v15 + non-temporal hint on the single-use P0 transpose loads and P1 x-row loads
# speedup vs baseline: 1.0187x; 1.0187x over previous
.LBB0_45:
	s_lshl_b32 s21, s16, 1
	s_lshl_b32 s22, s17, 1
	v_or_b32_e32 v15, s21, v1
	v_or_b32_e32 v21, s22, v2
	s_add_i32 s24, s22, 4
	s_add_i32 s23, s21, 4
	s_add_i32 s25, s21, 8
	s_add_i32 s26, s22, 8
	s_add_i32 s27, s21, 12
	s_add_i32 s29, s21, 16
	s_add_i32 s31, s21, 20
	s_add_i32 s34, s21, 24
	s_add_i32 s21, s21, 28
	v_add_lshl_u32 v6, v15, s3, 11
	v_add_lshl_u32 v24, v21, s2, 11
	v_or_b32_e32 v43, s24, v2
	s_add_i32 s28, s22, 12
	v_or_b32_e32 v42, s23, v1
	v_or_b32_e32 v44, s25, v1
	v_or_b32_e32 v45, s26, v2
	v_or_b32_e32 v46, s27, v1
	v_or_b32_e32 v48, s29, v1
	v_or_b32_e32 v50, s31, v1
	v_or_b32_e32 v52, s34, v1
	v_or_b32_e32 v54, s21, v1
	v_or_b32_e32 v22, v3, v6
	v_or_b32_e32 v6, v14, v24
	v_add_lshl_u32 v26, v43, s2, 11
	v_mov_b32_e32 v23, v7
	s_add_i32 s30, s22, 16
	v_or_b32_e32 v47, s28, v2
	v_add_lshl_u32 v24, v42, s3, 11
	v_add_lshl_u32 v28, v44, s3, 11
	v_add_lshl_u32 v56, v45, s2, 11
	v_add_lshl_u32 v30, v46, s3, 11
	v_add_lshl_u32 v32, v48, s3, 11
	v_add_lshl_u32 v34, v50, s3, 11
	v_add_lshl_u32 v36, v52, s3, 11
	v_add_lshl_u32 v40, v54, s3, 11
	v_lshl_add_u64 v[38:39], v[6:7], 2, s[12:13]
	v_or_b32_e32 v6, v14, v26
	v_mov_b32_e32 v25, v7
	s_add_i32 s33, s22, 20
	v_or_b32_e32 v49, s30, v2
	v_add_lshl_u32 v57, v47, s2, 11
	v_lshl_add_u64 v[22:23], v[22:23], 2, s[12:13]
	v_or_b32_e32 v24, v3, v24
	v_or_b32_e32 v26, v3, v28
	v_or_b32_e32 v28, v3, v30
	v_or_b32_e32 v30, v3, v32
	v_or_b32_e32 v32, v3, v34
	v_or_b32_e32 v34, v3, v36
	v_or_b32_e32 v36, v3, v40
	v_lshl_add_u64 v[40:41], v[6:7], 2, s[12:13]
	v_or_b32_e32 v6, v14, v56
	s_add_i32 s35, s22, 24
	v_or_b32_e32 v51, s33, v2
	v_add_lshl_u32 v58, v49, s2, 11
	v_lshl_add_u64 v[24:25], v[24:25], 2, s[12:13]
	global_load_dword v56, v[38:39], off nt
	global_load_dword v62, v[22:23], off nt
	global_load_dword v63, v[40:41], off nt
	global_load_dword v64, v[24:25], off nt
	v_lshl_add_u64 v[22:23], v[6:7], 2, s[12:13]
	v_or_b32_e32 v6, v14, v57
	v_mov_b32_e32 v27, v7
	v_mov_b32_e32 v29, v7
	s_add_i32 s22, s22, 28
	v_or_b32_e32 v53, s35, v2
	v_add_lshl_u32 v59, v51, s2, 11
	v_lshl_add_u64 v[24:25], v[6:7], 2, s[12:13]
	v_or_b32_e32 v6, v14, v58
	v_or_b32_e32 v55, s22, v2
	v_add_lshl_u32 v60, v53, s2, 11
	v_lshl_add_u64 v[26:27], v[26:27], 2, s[12:13]
	v_lshl_add_u64 v[28:29], v[28:29], 2, s[12:13]
	global_load_dword v57, v[22:23], off nt
	global_load_dword v58, v[26:27], off nt
	global_load_dword v65, v[24:25], off nt
	global_load_dword v66, v[28:29], off nt
	v_lshl_add_u64 v[22:23], v[6:7], 2, s[12:13]
	v_or_b32_e32 v6, v14, v59
	v_mov_b32_e32 v31, v7
	v_mov_b32_e32 v33, v7
	v_add_lshl_u32 v61, v55, s2, 11
	v_lshl_add_u64 v[24:25], v[6:7], 2, s[12:13]
	v_or_b32_e32 v6, v14, v60
	v_mov_b32_e32 v35, v7
	v_mov_b32_e32 v37, v7
	v_lshl_add_u64 v[30:31], v[30:31], 2, s[12:13]
	v_lshl_add_u64 v[32:33], v[32:33], 2, s[12:13]
	global_load_dword v59, v[22:23], off nt
	global_load_dword v60, v[30:31], off nt
	global_load_dword v67, v[24:25], off nt
	global_load_dword v68, v[32:33], off nt
	v_lshl_add_u64 v[22:23], v[6:7], 2, s[12:13]
	v_or_b32_e32 v6, v14, v61
	v_lshl_add_u64 v[34:35], v[34:35], 2, s[12:13]
	v_lshl_add_u64 v[36:37], v[36:37], 2, s[12:13]
	v_lshl_add_u64 v[24:25], v[6:7], 2, s[12:13]
	global_load_dword v6, v[22:23], off nt
	global_load_dword v61, v[34:35], off nt
	global_load_dword v69, v[24:25], off nt
	global_load_dword v70, v[36:37], off nt
	s_add_i32 s17, s17, 16
	s_add_i32 s16, s16, 16
	s_add_i32 s20, s20, -16
	v_mad_u64_u32 v[22:23], s[22:23], v21, s7, v[4:5]
	s_cmp_lg_u32 s20, 0
	v_mad_u64_u32 v[24:25], s[22:23], v15, s7, v[4:5]
	v_mad_u64_u32 v[26:27], s[22:23], v43, s7, v[4:5]
	v_mad_u64_u32 v[28:29], s[22:23], v42, s7, v[4:5]
	v_mad_u64_u32 v[30:31], s[22:23], v45, s7, v[4:5]
	v_mad_u64_u32 v[32:33], s[22:23], v44, s7, v[4:5]
	v_mad_u64_u32 v[34:35], s[22:23], v47, s7, v[4:5]
	v_mad_u64_u32 v[36:37], s[22:23], v46, s7, v[4:5]
	v_mad_u64_u32 v[38:39], s[22:23], v49, s7, v[4:5]
	v_mad_u64_u32 v[40:41], s[22:23], v48, s7, v[4:5]
	v_mad_u64_u32 v[42:43], s[22:23], v51, s7, v[4:5]
	v_mad_u64_u32 v[44:45], s[22:23], v50, s7, v[4:5]
	v_mad_u64_u32 v[46:47], s[22:23], v53, s7, v[4:5]
	v_mad_u64_u32 v[48:49], s[22:23], v52, s7, v[4:5]
	v_mad_u64_u32 v[50:51], s[22:23], v55, s7, v[4:5]
	v_mad_u64_u32 v[52:53], s[22:23], v54, s7, v[4:5]
	s_waitcnt vmcnt(15)
	ds_write_b32 v22, v56
	s_waitcnt vmcnt(14)
	ds_write_b32 v24, v62
	s_waitcnt vmcnt(13)
	ds_write_b32 v26, v63
	s_waitcnt vmcnt(12)
	ds_write_b32 v28, v64
	s_waitcnt vmcnt(11)
	ds_write_b32 v30, v57
	s_waitcnt vmcnt(10)
	ds_write_b32 v32, v58
	s_waitcnt vmcnt(9)
	ds_write_b32 v34, v65
	s_waitcnt vmcnt(8)
	ds_write_b32 v36, v66
	s_waitcnt vmcnt(7)
	ds_write_b32 v38, v59
	s_waitcnt vmcnt(6)
	ds_write_b32 v40, v60
	s_waitcnt vmcnt(5)
	ds_write_b32 v42, v67
	s_waitcnt vmcnt(4)
	ds_write_b32 v44, v68
	s_waitcnt vmcnt(3)
	ds_write_b32 v46, v6
	s_waitcnt vmcnt(2)
	ds_write_b32 v48, v61
	s_waitcnt vmcnt(1)
	ds_write_b32 v50, v69
	s_waitcnt vmcnt(0)
	ds_write_b32 v52, v70
	s_cbranch_scc1 .LBB0_45
	s_waitcnt lgkmcnt(0)
	ds_read2_b32 v[14:15], v17 offset1:8
	ds_read2_b32 v[28:29], v17 offset0:33 offset1:41
	ds_read2_b32 v[30:31], v17 offset0:66 offset1:74
	ds_read2_b32 v[32:33], v17 offset0:99 offset1:107
	ds_read2_b32 v[34:35], v17 offset0:132 offset1:140
	ds_read2_b32 v[36:37], v17 offset0:165 offset1:173
	s_waitcnt lgkmcnt(5)
	v_bfe_u32 v3, v14, 16, 1
	v_add3_u32 v3, v14, v3, s8
	s_waitcnt lgkmcnt(4)
	v_bfe_u32 v6, v28, 16, 1
	v_lshrrev_b32_e32 v3, 16, v3
	v_add3_u32 v6, v28, v6, s8
	v_and_or_b32 v22, v6, s9, v3
	s_waitcnt lgkmcnt(3)
	v_bfe_u32 v3, v30, 16, 1
	v_add3_u32 v3, v30, v3, s8
	s_waitcnt lgkmcnt(2)
	v_bfe_u32 v6, v32, 16, 1
	ds_read2_b32 v[38:39], v17 offset0:198 offset1:206
	v_lshrrev_b32_e32 v3, 16, v3
	v_add3_u32 v6, v32, v6, s8
	ds_read2_b32 v[40:41], v17 offset0:231 offset1:239
	v_and_or_b32 v23, v6, s9, v3
	s_waitcnt lgkmcnt(3)
	v_bfe_u32 v3, v34, 16, 1
	v_add3_u32 v3, v34, v3, s8
	s_waitcnt lgkmcnt(2)
	v_bfe_u32 v6, v36, 16, 1
	v_lshrrev_b32_e32 v3, 16, v3
	v_add3_u32 v6, v36, v6, s8
	v_and_or_b32 v24, v6, s9, v3
	s_waitcnt lgkmcnt(1)
	v_bfe_u32 v3, v38, 16, 1
	v_add3_u32 v3, v38, v3, s8
	s_waitcnt lgkmcnt(0)
	v_bfe_u32 v6, v40, 16, 1
	v_lshrrev_b32_e32 v3, 16, v3
	v_add3_u32 v6, v40, v6, s8
	s_mov_b32 s3, s6
	v_and_or_b32 v25, v6, s9, v3
	v_or_b32_e32 v3, s15, v16
	v_lshl_add_u64 v[26:27], s[2:3], 1, v[8:9]
	v_lshlrev_b32_e32 v6, 12, v3
	v_bfe_u32 v3, v15, 16, 1
	v_lshl_add_u64 v[42:43], v[26:27], 0, v[6:7]
	v_add3_u32 v3, v15, v3, s8
	v_bfe_u32 v6, v29, 16, 1
	v_lshrrev_b32_e32 v3, 16, v3
	v_add3_u32 v6, v29, v6, s8
	global_store_dwordx4 v[42:43], v[22:25], off
	ds_read2_b32 v[14:15], v17 offset0:16 offset1:24
	s_nop 0
	v_and_or_b32 v22, v6, s9, v3
	v_bfe_u32 v3, v31, 16, 1
	v_add3_u32 v3, v31, v3, s8
	v_bfe_u32 v6, v33, 16, 1
	v_lshrrev_b32_e32 v3, 16, v3
	v_add3_u32 v6, v33, v6, s8
	v_and_or_b32 v23, v6, s9, v3
	v_bfe_u32 v3, v35, 16, 1
	v_add3_u32 v3, v35, v3, s8
	v_bfe_u32 v6, v37, 16, 1
	v_lshrrev_b32_e32 v3, 16, v3
	v_add3_u32 v6, v37, v6, s8
	v_and_or_b32 v24, v6, s9, v3
	v_bfe_u32 v3, v39, 16, 1
	v_add3_u32 v3, v39, v3, s8
	v_bfe_u32 v6, v41, 16, 1
	v_lshrrev_b32_e32 v3, 16, v3
	v_add3_u32 v6, v41, v6, s8
	v_and_or_b32 v25, v6, s9, v3
	v_or_b32_e32 v3, s15, v18
	v_lshlrev_b32_e32 v6, 12, v3
	v_lshl_add_u64 v[28:29], v[26:27], 0, v[6:7]
	global_store_dwordx4 v[28:29], v[22:25], off
	ds_read2_b32 v[28:29], v17 offset0:49 offset1:57
	ds_read2_b32 v[30:31], v17 offset0:82 offset1:90
	ds_read2_b32 v[32:33], v17 offset0:115 offset1:123
	s_waitcnt lgkmcnt(3)
	v_bfe_u32 v3, v14, 16, 1
	v_add3_u32 v3, v14, v3, s8
	s_waitcnt lgkmcnt(2)
	v_bfe_u32 v6, v28, 16, 1
	ds_read2_b32 v[34:35], v17 offset0:148 offset1:156
	v_lshrrev_b32_e32 v3, 16, v3
	v_add3_u32 v6, v28, v6, s8
	ds_read2_b32 v[36:37], v17 offset0:181 offset1:189
	v_and_or_b32 v22, v6, s9, v3
	s_waitcnt lgkmcnt(3)
	v_bfe_u32 v3, v30, 16, 1
	v_add3_u32 v3, v30, v3, s8
	s_waitcnt lgkmcnt(2)
	v_bfe_u32 v6, v32, 16, 1
	ds_read2_b32 v[38:39], v17 offset0:214 offset1:222
	v_lshrrev_b32_e32 v3, 16, v3
	v_add3_u32 v6, v32, v6, s8
	ds_read2_b32 v[40:41], v17 offset0:247 offset1:255
	v_and_or_b32 v23, v6, s9, v3
	s_waitcnt lgkmcnt(3)
	v_bfe_u32 v3, v34, 16, 1
	v_add3_u32 v3, v34, v3, s8
	s_waitcnt lgkmcnt(2)
	v_bfe_u32 v6, v36, 16, 1
	v_lshrrev_b32_e32 v3, 16, v3
	v_add3_u32 v6, v36, v6, s8
	v_and_or_b32 v24, v6, s9, v3
	s_waitcnt lgkmcnt(1)
	v_bfe_u32 v3, v38, 16, 1
	v_add3_u32 v3, v38, v3, s8
	s_waitcnt lgkmcnt(0)
	v_bfe_u32 v6, v40, 16, 1
	v_lshrrev_b32_e32 v3, 16, v3
	v_add3_u32 v6, v40, v6, s8
	v_and_or_b32 v25, v6, s9, v3
	v_or_b32_e32 v3, s15, v19
	v_lshlrev_b32_e32 v6, 12, v3
	v_bfe_u32 v3, v15, 16, 1
	v_lshl_add_u64 v[42:43], v[26:27], 0, v[6:7]
	v_add3_u32 v3, v15, v3, s8
	v_bfe_u32 v6, v29, 16, 1
	v_lshrrev_b32_e32 v3, 16, v3
	v_add3_u32 v6, v29, v6, s8
	global_store_dwordx4 v[42:43], v[22:25], off
	s_nop 1
	v_and_or_b32 v22, v6, s9, v3
	v_bfe_u32 v3, v31, 16, 1
	v_add3_u32 v3, v31, v3, s8
	v_bfe_u32 v6, v33, 16, 1
	v_lshrrev_b32_e32 v3, 16, v3
	v_add3_u32 v6, v33, v6, s8
	v_and_or_b32 v23, v6, s9, v3
	v_bfe_u32 v3, v35, 16, 1
	v_add3_u32 v3, v35, v3, s8
	v_bfe_u32 v6, v37, 16, 1
	v_lshrrev_b32_e32 v3, 16, v3
	v_add3_u32 v6, v37, v6, s8
	v_and_or_b32 v24, v6, s9, v3
	v_bfe_u32 v3, v39, 16, 1
	v_add3_u32 v3, v39, v3, s8
	v_bfe_u32 v6, v41, 16, 1
	v_lshrrev_b32_e32 v3, 16, v3
	v_add3_u32 v6, v41, v6, s8
	v_and_or_b32 v25, v6, s9, v3
	v_or_b32_e32 v3, s15, v20
	v_lshlrev_b32_e32 v6, 12, v3
	v_lshl_add_u64 v[14:15], v[26:27], 0, v[6:7]
	global_store_dwordx4 v[14:15], v[22:25], off
	s_waitcnt lgkmcnt(0)
	s_branch .LBB0_42

.LBB0_49:
	s_lshl_b32 s21, s16, 1
	s_lshl_b32 s22, s17, 1
	v_or_b32_e32 v3, s21, v1
	v_or_b32_e32 v6, s22, v2
	s_add_i32 s23, s21, 4
	s_add_i32 s24, s22, 4
	s_add_i32 s25, s21, 8
	s_add_i32 s26, s22, 8
	s_add_i32 s27, s21, 12
	s_add_i32 s28, s22, 12
	s_add_i32 s29, s21, 16
	s_add_i32 s30, s22, 16
	s_add_i32 s31, s21, 20
	s_add_i32 s33, s22, 20
	s_add_i32 s34, s21, 24
	s_add_i32 s35, s22, 24
	s_add_i32 s21, s21, 28
	s_add_i32 s22, s22, 28
	v_add_u32_e32 v21, s3, v3
	v_add_u32_e32 v22, s2, v6
	v_or_b32_e32 v54, s23, v1
	v_or_b32_e32 v55, s24, v2
	v_or_b32_e32 v56, s25, v1
	v_or_b32_e32 v57, s26, v2
	v_or_b32_e32 v58, s27, v1
	v_or_b32_e32 v59, s28, v2
	v_or_b32_e32 v60, s29, v1
	v_or_b32_e32 v61, s30, v2
	v_or_b32_e32 v62, s31, v1
	v_or_b32_e32 v63, s33, v2
	v_or_b32_e32 v64, s34, v1
	v_or_b32_e32 v65, s35, v2
	v_or_b32_e32 v66, s21, v1
	v_or_b32_e32 v67, s22, v2
	v_mad_i64_i32 v[22:23], s[22:23], v22, s14, v[14:15]
	v_mad_i64_i32 v[24:25], s[22:23], v21, s14, v[14:15]
	v_add_u32_e32 v21, s3, v54
	v_add_u32_e32 v26, s2, v55
	v_add_u32_e32 v32, s3, v56
	v_add_u32_e32 v30, s2, v57
	v_add_u32_e32 v36, s3, v58
	v_add_u32_e32 v34, s2, v59
	v_add_u32_e32 v40, s3, v60
	v_add_u32_e32 v38, s2, v61
	v_add_u32_e32 v44, s3, v62
	v_add_u32_e32 v42, s2, v63
	v_add_u32_e32 v48, s3, v64
	v_add_u32_e32 v46, s2, v65
	v_add_u32_e32 v52, s3, v66
	v_add_u32_e32 v50, s2, v67
	v_mad_i64_i32 v[26:27], s[22:23], v26, s14, v[14:15]
	v_mad_i64_i32 v[28:29], s[22:23], v21, s14, v[14:15]
	v_mad_i64_i32 v[30:31], s[22:23], v30, s14, v[14:15]
	v_mad_i64_i32 v[32:33], s[22:23], v32, s14, v[14:15]
	v_mad_i64_i32 v[34:35], s[22:23], v34, s14, v[14:15]
	v_mad_i64_i32 v[36:37], s[22:23], v36, s14, v[14:15]
	v_mad_i64_i32 v[38:39], s[22:23], v38, s14, v[14:15]
	v_mad_i64_i32 v[40:41], s[22:23], v40, s14, v[14:15]
	v_mad_i64_i32 v[42:43], s[22:23], v42, s14, v[14:15]
	v_mad_i64_i32 v[44:45], s[22:23], v44, s14, v[14:15]
	v_mad_i64_i32 v[46:47], s[22:23], v46, s14, v[14:15]
	v_mad_i64_i32 v[48:49], s[22:23], v48, s14, v[14:15]
	v_mad_i64_i32 v[50:51], s[22:23], v50, s14, v[14:15]
	v_mad_i64_i32 v[52:53], s[22:23], v52, s14, v[14:15]
	global_load_dword v21, v[22:23], off nt
	global_load_dword v68, v[24:25], off nt
	global_load_dword v69, v[26:27], off nt
	global_load_dword v70, v[28:29], off nt
	global_load_dword v71, v[30:31], off nt
	global_load_dword v72, v[32:33], off nt
	global_load_dword v73, v[34:35], off nt
	global_load_dword v74, v[36:37], off nt
	global_load_dword v75, v[38:39], off nt
	global_load_dword v76, v[40:41], off nt
	global_load_dword v77, v[42:43], off nt
	global_load_dword v78, v[44:45], off nt
	global_load_dword v79, v[46:47], off nt
	global_load_dword v80, v[48:49], off nt
	global_load_dword v81, v[50:51], off nt
	global_load_dword v82, v[52:53], off nt
	s_add_i32 s17, s17, 16
	s_add_i32 s16, s16, 16
	s_add_i32 s20, s20, -16
	v_mad_u64_u32 v[22:23], s[22:23], v6, s7, v[4:5]
	s_cmp_lg_u32 s20, 0
	v_mad_u64_u32 v[24:25], s[22:23], v3, s7, v[4:5]
	v_mad_u64_u32 v[26:27], s[22:23], v55, s7, v[4:5]
	v_mad_u64_u32 v[28:29], s[22:23], v54, s7, v[4:5]
	v_mad_u64_u32 v[30:31], s[22:23], v57, s7, v[4:5]
	v_mad_u64_u32 v[32:33], s[22:23], v56, s7, v[4:5]
	v_mad_u64_u32 v[34:35], s[22:23], v59, s7, v[4:5]
	v_mad_u64_u32 v[36:37], s[22:23], v58, s7, v[4:5]
	v_mad_u64_u32 v[38:39], s[22:23], v61, s7, v[4:5]
	v_mad_u64_u32 v[40:41], s[22:23], v60, s7, v[4:5]
	v_mad_u64_u32 v[42:43], s[22:23], v63, s7, v[4:5]
	v_mad_u64_u32 v[44:45], s[22:23], v62, s7, v[4:5]
	v_mad_u64_u32 v[46:47], s[22:23], v65, s7, v[4:5]
	v_mad_u64_u32 v[48:49], s[22:23], v64, s7, v[4:5]
	v_mad_u64_u32 v[50:51], s[22:23], v67, s7, v[4:5]
	v_mad_u64_u32 v[52:53], s[22:23], v66, s7, v[4:5]
	s_waitcnt vmcnt(15)
	ds_write_b32 v22, v21
	s_waitcnt vmcnt(14)
	ds_write_b32 v24, v68
	s_waitcnt vmcnt(13)
	ds_write_b32 v26, v69
	s_waitcnt vmcnt(12)
	ds_write_b32 v28, v70
	s_waitcnt vmcnt(11)
	ds_write_b32 v30, v71
	s_waitcnt vmcnt(10)
	ds_write_b32 v32, v72
	s_waitcnt vmcnt(9)
	ds_write_b32 v34, v73
	s_waitcnt vmcnt(8)
	ds_write_b32 v36, v74
	s_waitcnt vmcnt(7)
	ds_write_b32 v38, v75
	s_waitcnt vmcnt(6)
	ds_write_b32 v40, v76
	s_waitcnt vmcnt(5)
	ds_write_b32 v42, v77
	s_waitcnt vmcnt(4)
	ds_write_b32 v44, v78
	s_waitcnt vmcnt(3)
	ds_write_b32 v46, v79
	s_waitcnt vmcnt(2)
	ds_write_b32 v48, v80
	s_waitcnt vmcnt(1)
	ds_write_b32 v50, v81
	s_waitcnt vmcnt(0)
	ds_write_b32 v52, v82
	s_cbranch_scc1 .LBB0_49
	s_waitcnt lgkmcnt(0)
	ds_read2_b32 v[14:15], v17 offset1:8
	ds_read2_b32 v[28:29], v17 offset0:33 offset1:41
	ds_read2_b32 v[30:31], v17 offset0:66 offset1:74
	ds_read2_b32 v[32:33], v17 offset0:99 offset1:107
	ds_read2_b32 v[34:35], v17 offset0:132 offset1:140
	ds_read2_b32 v[36:37], v17 offset0:165 offset1:173
	s_waitcnt lgkmcnt(5)
	v_bfe_u32 v3, v14, 16, 1
	v_add3_u32 v3, v14, v3, s8
	s_waitcnt lgkmcnt(4)
	v_bfe_u32 v6, v28, 16, 1
	v_lshrrev_b32_e32 v3, 16, v3
	v_add3_u32 v6, v28, v6, s8
	v_and_or_b32 v22, v6, s9, v3
	s_waitcnt lgkmcnt(3)
	v_bfe_u32 v3, v30, 16, 1
	v_add3_u32 v3, v30, v3, s8
	s_waitcnt lgkmcnt(2)
	v_bfe_u32 v6, v32, 16, 1
	ds_read2_b32 v[38:39], v17 offset0:198 offset1:206
	v_lshrrev_b32_e32 v3, 16, v3
	v_add3_u32 v6, v32, v6, s8
	ds_read2_b32 v[40:41], v17 offset0:231 offset1:239
	v_and_or_b32 v23, v6, s9, v3
	s_waitcnt lgkmcnt(3)
	v_bfe_u32 v3, v34, 16, 1
	v_add3_u32 v3, v34, v3, s8
	s_waitcnt lgkmcnt(2)
	v_bfe_u32 v6, v36, 16, 1
	v_lshrrev_b32_e32 v3, 16, v3
	v_add3_u32 v6, v36, v6, s8
	v_and_or_b32 v24, v6, s9, v3
	s_waitcnt lgkmcnt(1)
	v_bfe_u32 v3, v38, 16, 1
	v_add3_u32 v3, v38, v3, s8
	s_waitcnt lgkmcnt(0)
	v_bfe_u32 v6, v40, 16, 1
	v_lshrrev_b32_e32 v3, 16, v3
	v_add3_u32 v6, v40, v6, s8
	v_or_b32_e32 v42, s15, v16
	s_ashr_i32 s3, s2, 31
	v_and_or_b32 v25, v6, s9, v3
	v_ashrrev_i32_e32 v43, 31, v42
	v_bfe_u32 v3, v15, 16, 1
	v_lshl_add_u64 v[26:27], s[2:3], 1, v[12:13]
	v_lshlrev_b64 v[42:43], 12, v[42:43]
	v_add3_u32 v3, v15, v3, s8
	v_bfe_u32 v6, v29, 16, 1
	v_lshl_add_u64 v[42:43], v[26:27], 0, v[42:43]
	v_lshrrev_b32_e32 v3, 16, v3
	v_add3_u32 v6, v29, v6, s8
	global_store_dwordx4 v[42:43], v[22:25], off
	v_or_b32_e32 v14, s15, v18
	v_ashrrev_i32_e32 v15, 31, v14
	v_and_or_b32 v22, v6, s9, v3
	v_bfe_u32 v3, v31, 16, 1
	v_add3_u32 v3, v31, v3, s8
	v_bfe_u32 v6, v33, 16, 1
	v_lshrrev_b32_e32 v3, 16, v3
	v_add3_u32 v6, v33, v6, s8
	v_and_or_b32 v23, v6, s9, v3
	v_bfe_u32 v3, v35, 16, 1
	v_add3_u32 v3, v35, v3, s8
	v_bfe_u32 v6, v37, 16, 1
	v_lshrrev_b32_e32 v3, 16, v3
	v_add3_u32 v6, v37, v6, s8
	v_and_or_b32 v24, v6, s9, v3
	v_bfe_u32 v3, v39, 16, 1
	v_add3_u32 v3, v39, v3, s8
	v_bfe_u32 v6, v41, 16, 1
	v_lshrrev_b32_e32 v3, 16, v3
	v_add3_u32 v6, v41, v6, s8
	v_lshlrev_b64 v[14:15], 12, v[14:15]
	v_and_or_b32 v25, v6, s9, v3
	ds_read2_b32 v[28:29], v17 offset0:16 offset1:24
	v_lshl_add_u64 v[14:15], v[26:27], 0, v[14:15]
	global_store_dwordx4 v[14:15], v[22:25], off
	ds_read2_b32 v[14:15], v17 offset0:49 offset1:57
	ds_read2_b32 v[30:31], v17 offset0:82 offset1:90
	ds_read2_b32 v[32:33], v17 offset0:115 offset1:123
	s_waitcnt lgkmcnt(3)
	v_bfe_u32 v3, v28, 16, 1
	v_add3_u32 v3, v28, v3, s8
	s_waitcnt lgkmcnt(2)
	v_bfe_u32 v6, v14, 16, 1
	ds_read2_b32 v[34:35], v17 offset0:148 offset1:156
	v_lshrrev_b32_e32 v3, 16, v3
	v_add3_u32 v6, v14, v6, s8
	ds_read2_b32 v[36:37], v17 offset0:181 offset1:189
	v_and_or_b32 v22, v6, s9, v3
	s_waitcnt lgkmcnt(3)
	v_bfe_u32 v3, v30, 16, 1
	v_add3_u32 v3, v30, v3, s8
	s_waitcnt lgkmcnt(2)
	v_bfe_u32 v6, v32, 16, 1
	ds_read2_b32 v[38:39], v17 offset0:214 offset1:222
	v_lshrrev_b32_e32 v3, 16, v3
	v_add3_u32 v6, v32, v6, s8
	ds_read2_b32 v[40:41], v17 offset0:247 offset1:255
	v_and_or_b32 v23, v6, s9, v3
	s_waitcnt lgkmcnt(3)
	v_bfe_u32 v3, v34, 16, 1
	v_add3_u32 v3, v34, v3, s8
	s_waitcnt lgkmcnt(2)
	v_bfe_u32 v6, v36, 16, 1
	v_lshrrev_b32_e32 v3, 16, v3
	v_add3_u32 v6, v36, v6, s8
	v_and_or_b32 v24, v6, s9, v3
	s_waitcnt lgkmcnt(1)
	v_bfe_u32 v3, v38, 16, 1
	v_add3_u32 v3, v38, v3, s8
	s_waitcnt lgkmcnt(0)
	v_bfe_u32 v6, v40, 16, 1
	v_lshrrev_b32_e32 v3, 16, v3
	v_add3_u32 v6, v40, v6, s8
	v_or_b32_e32 v42, s15, v19
	v_and_or_b32 v25, v6, s9, v3
	v_ashrrev_i32_e32 v43, 31, v42
	v_bfe_u32 v3, v29, 16, 1
	v_lshlrev_b64 v[42:43], 12, v[42:43]
	v_add3_u32 v3, v29, v3, s8
	v_bfe_u32 v6, v15, 16, 1
	v_lshl_add_u64 v[42:43], v[26:27], 0, v[42:43]
	v_lshrrev_b32_e32 v3, 16, v3
	v_add3_u32 v6, v15, v6, s8
	global_store_dwordx4 v[42:43], v[22:25], off
	v_or_b32_e32 v14, s15, v20
	v_ashrrev_i32_e32 v15, 31, v14
	v_and_or_b32 v22, v6, s9, v3
	v_bfe_u32 v3, v31, 16, 1
	v_add3_u32 v3, v31, v3, s8
	v_bfe_u32 v6, v33, 16, 1
	v_lshrrev_b32_e32 v3, 16, v3
	v_add3_u32 v6, v33, v6, s8
	v_and_or_b32 v23, v6, s9, v3
	v_bfe_u32 v3, v35, 16, 1
	v_add3_u32 v3, v35, v3, s8
	v_bfe_u32 v6, v37, 16, 1
	v_lshrrev_b32_e32 v3, 16, v3
	v_add3_u32 v6, v37, v6, s8
	v_and_or_b32 v24, v6, s9, v3
	v_bfe_u32 v3, v39, 16, 1
	v_add3_u32 v3, v39, v3, s8
	v_bfe_u32 v6, v41, 16, 1
	v_lshrrev_b32_e32 v3, 16, v3
	v_add3_u32 v6, v41, v6, s8
	v_lshlrev_b64 v[14:15], 12, v[14:15]
	v_and_or_b32 v25, v6, s9, v3
	v_lshl_add_u64 v[14:15], v[26:27], 0, v[14:15]
	global_store_dwordx4 v[14:15], v[22:25], off
	s_waitcnt lgkmcnt(0)
	s_branch .LBB0_42

.LBB0_112:
	s_mov_b32 s44, 0x1000
	s_mov_b32 s45, 0
	v_lshl_add_u64 v[144:145], v[20:21], 0, s[44:45]
	global_load_dwordx4 v[112:115], v[20:21], off offset:-1024 nt
	global_load_dwordx4 v[116:119], v[20:21], off nt
	global_load_dwordx4 v[120:123], v[20:21], off offset:1024 nt
	global_load_dwordx4 v[124:127], v[20:21], off offset:2048 nt
	global_load_dwordx4 v[128:131], v[20:21], off offset:3072 nt
	global_load_dwordx4 v[132:135], v[144:145], off nt
	global_load_dwordx4 v[136:139], v[144:145], off offset:1024 nt
	global_load_dwordx4 v[140:143], v[144:145], off offset:2048 nt
	v_add_u32_e32 v29, s17, v28
	v_add_u32_e32 v90, s17, v1
	v_add_u32_e32 v98, 0x10000, v29
	v_add_u32_e32 v94, 0x12000, v29
	v_add_u32_e32 v102, 0x12400, v29
	ds_read_b128 v[30:33], v90
	ds_read_b128 v[34:37], v90 offset:1024
	ds_read_b128 v[38:41], v90 offset:8192
	ds_read_b128 v[42:45], v90 offset:9216
	ds_read_b128 v[46:49], v90 offset:16384
	ds_read_b128 v[50:53], v90 offset:17408
	ds_read_b128 v[54:57], v90 offset:24576
	ds_read_b128 v[58:61], v90 offset:25600
	ds_read_b128 v[62:65], v90 offset:32768
	ds_read_b128 v[66:69], v90 offset:33792
	ds_read_b128 v[70:73], v90 offset:40960
	ds_read_b128 v[74:77], v90 offset:41984
	ds_read_b128 v[78:81], v90 offset:49152
	ds_read_b128 v[82:85], v90 offset:50176
	ds_read_b128 v[86:89], v90 offset:57344
	ds_read_b128 v[90:93], v90 offset:58368
	v_add_u32_e32 v29, 0x10400, v29
	ds_read_b128 v[94:97], v94
	ds_read_b128 v[98:101], v98
	ds_read_b128 v[102:105], v102
	ds_read_b128 v[106:109], v29
	s_waitcnt lgkmcnt(14)
	v_pk_mov_b32 v[110:111], v[30:31], v[38:39] op_sel:[1,0]
	v_mov_b32_e32 v31, v39
	v_pk_mov_b32 v[38:39], v[32:33], v[40:41] op_sel:[1,0]
	v_mov_b32_e32 v33, v41
	s_waitcnt lgkmcnt(13)
	v_pk_mov_b32 v[40:41], v[46:47], v[54:55] op_sel:[1,0]
	v_mov_b32_e32 v47, v55
	v_pk_mov_b32 v[54:55], v[48:49], v[56:57] op_sel:[1,0]
	v_mov_b32_e32 v49, v57
	s_waitcnt lgkmcnt(9)
	v_pk_mov_b32 v[56:57], v[62:63], v[70:71] op_sel:[1,0]
	v_mov_b32_e32 v63, v71
	v_pk_mov_b32 v[70:71], v[64:65], v[72:73] op_sel:[1,0]
	v_mov_b32_e32 v65, v73
	v_pk_mov_b32 v[72:73], v[34:35], v[42:43] op_sel:[1,0]
	v_mov_b32_e32 v35, v43
	v_pk_mov_b32 v[42:43], v[36:37], v[44:45] op_sel:[1,0]
	v_mov_b32_e32 v37, v45
	v_pk_mov_b32 v[44:45], v[50:51], v[58:59] op_sel:[1,0]
	v_mov_b32_e32 v51, v59
	v_pk_mov_b32 v[58:59], v[52:53], v[60:61] op_sel:[1,0]
	v_mov_b32_e32 v53, v61
	s_waitcnt lgkmcnt(8)
	v_pk_mov_b32 v[60:61], v[66:67], v[74:75] op_sel:[1,0]
	v_mov_b32_e32 v67, v75
	v_pk_mov_b32 v[74:75], v[68:69], v[76:77] op_sel:[1,0]
	v_mov_b32_e32 v69, v77
	s_addk_i32 s17, 0x800
	s_waitcnt vmcnt(7) lgkmcnt(2)
	v_pk_fma_f32 v[96:97], v[114:115], v[96:97], v[100:101]
	v_pk_fma_f32 v[94:95], v[112:113], v[94:95], v[98:99]
	v_and_b32_sdwa v5, v97, v6 dst_sel:DWORD dst_unused:UNUSED_PAD src0_sel:WORD_1 src1_sel:DWORD
	v_and_b32_sdwa v3, v95, v6 dst_sel:DWORD dst_unused:UNUSED_PAD src0_sel:WORD_1 src1_sel:DWORD
	v_and_b32_sdwa v2, v94, v6 dst_sel:DWORD dst_unused:UNUSED_PAD src0_sel:WORD_1 src1_sel:DWORD
	v_and_b32_sdwa v4, v96, v6 dst_sel:DWORD dst_unused:UNUSED_PAD src0_sel:WORD_1 src1_sel:DWORD
	v_add3_u32 v3, v95, v3, s16
	v_add3_u32 v5, v97, v5, s16
	v_add3_u32 v2, v94, v2, s16
	v_add3_u32 v4, v96, v4, s16
	v_and_b32_e32 v5, 0xffff0000, v5
	v_and_b32_e32 v29, 0xffff0000, v3
	v_or_b32_sdwa v3, v5, v4 dst_sel:DWORD dst_unused:UNUSED_PAD src0_sel:DWORD src1_sel:WORD_1
	v_or_b32_sdwa v2, v29, v2 dst_sel:DWORD dst_unused:UNUSED_PAD src0_sel:DWORD src1_sel:WORD_1
	global_store_dwordx2 v[22:23], v[2:3], off
	v_pk_mul_f32 v[30:31], v[94:95], v[30:31]
	v_pk_mul_f32 v[32:33], v[96:97], v[32:33]
	v_pk_mul_f32 v[46:47], v[94:95], v[46:47]
	v_pk_mul_f32 v[48:49], v[96:97], v[48:49]
	v_pk_mul_f32 v[88:89], v[96:97], v[88:89]
	v_pk_mul_f32 v[86:87], v[94:95], v[86:87]
	v_mul_f32_e32 v76, v95, v79
	v_mul_f32_e32 v98, v97, v81
	v_pk_fma_f32 v[30:31], v[94:95], v[110:111], v[30:31] op_sel:[1,0,0] op_sel_hi:[0,1,1]
	v_pk_fma_f32 v[40:41], v[94:95], v[40:41], v[46:47] op_sel:[1,0,0] op_sel_hi:[0,1,1]
	v_pk_fma_f32 v[32:33], v[96:97], v[38:39], v[32:33] op_sel:[1,0,0] op_sel_hi:[0,1,1]
	v_pk_fma_f32 v[38:39], v[96:97], v[54:55], v[48:49] op_sel:[1,0,0] op_sel_hi:[0,1,1]
	v_pk_mov_b32 v[54:55], v[86:87], v[88:89] op_sel:[1,0]
	v_mov_b32_e32 v87, v89
	v_pk_mul_f32 v[62:63], v[94:95], v[62:63]
	v_pk_mul_f32 v[64:65], v[96:97], v[64:65]
	v_pk_fma_f32 v[76:77], v[94:95], v[78:79], v[76:77] op_sel_hi:[1,1,0]
	v_pk_fma_f32 v[78:79], v[96:97], v[80:81], v[98:99] op_sel_hi:[1,1,0]
	v_pk_add_f32 v[30:31], v[30:31], v[32:33]
	v_pk_add_f32 v[32:33], v[40:41], v[38:39]
	v_pk_add_f32 v[40:41], v[54:55], v[86:87]
	v_pk_fma_f32 v[46:47], v[94:95], v[56:57], v[62:63] op_sel:[1,0,0] op_sel_hi:[0,1,1]
	v_pk_fma_f32 v[48:49], v[96:97], v[70:71], v[64:65] op_sel:[1,0,0] op_sel_hi:[0,1,1]
	v_mov_b32_e32 v77, v40
	v_mov_b32_e32 v79, v41
	v_pk_add_f32 v[38:39], v[46:47], v[48:49]
	v_pk_add_f32 v[26:27], v[26:27], v[30:31]
	v_pk_add_f32 v[30:31], v[76:77], v[78:79]
	v_pk_add_f32 v[24:25], v[24:25], v[32:33]
	v_pk_add_f32 v[18:19], v[18:19], v[38:39]
	v_pk_add_f32 v[16:17], v[16:17], v[30:31]
	v_lshl_add_u64 v[20:21], v[20:21], 0, s[40:41]
	s_waitcnt vmcnt(7) lgkmcnt(0)
	v_pk_fma_f32 v[4:5], v[118:119], v[104:105], v[108:109]
	v_pk_fma_f32 v[2:3], v[116:117], v[102:103], v[106:107]
	v_and_b32_sdwa v49, v5, v6 dst_sel:DWORD dst_unused:UNUSED_PAD src0_sel:WORD_1 src1_sel:DWORD
	v_and_b32_sdwa v47, v2, v6 dst_sel:DWORD dst_unused:UNUSED_PAD src0_sel:WORD_1 src1_sel:DWORD
	v_and_b32_sdwa v29, v4, v6 dst_sel:DWORD dst_unused:UNUSED_PAD src0_sel:WORD_1 src1_sel:DWORD
	v_and_b32_sdwa v54, v3, v6 dst_sel:DWORD dst_unused:UNUSED_PAD src0_sel:WORD_1 src1_sel:DWORD
	v_pk_mul_f32 v[30:31], v[2:3], v[34:35]
	v_pk_mul_f32 v[32:33], v[4:5], v[36:37]
	v_pk_mul_f32 v[34:35], v[2:3], v[50:51]
	v_pk_mul_f32 v[36:37], v[4:5], v[52:53]
	v_pk_mul_f32 v[38:39], v[2:3], v[66:67]
	v_pk_mul_f32 v[40:41], v[4:5], v[68:69]
	v_mul_f32_e32 v46, v3, v83
	v_mul_f32_e32 v48, v5, v85
	v_pk_mul_f32 v[50:51], v[4:5], v[92:93]
	v_pk_mul_f32 v[52:53], v[2:3], v[90:91]
	v_add3_u32 v47, v2, v47, s16
	v_add3_u32 v49, v5, v49, s16
	v_add3_u32 v29, v4, v29, s16
	v_add3_u32 v54, v3, v54, s16
	v_pk_fma_f32 v[30:31], v[2:3], v[72:73], v[30:31] op_sel:[1,0,0] op_sel_hi:[0,1,1]
	v_pk_fma_f32 v[32:33], v[4:5], v[42:43], v[32:33] op_sel:[1,0,0] op_sel_hi:[0,1,1]
	v_pk_fma_f32 v[34:35], v[2:3], v[44:45], v[34:35] op_sel:[1,0,0] op_sel_hi:[0,1,1]
	v_pk_fma_f32 v[36:37], v[4:5], v[58:59], v[36:37] op_sel:[1,0,0] op_sel_hi:[0,1,1]
	v_pk_fma_f32 v[38:39], v[2:3], v[60:61], v[38:39] op_sel:[1,0,0] op_sel_hi:[0,1,1]
	v_pk_fma_f32 v[40:41], v[4:5], v[74:75], v[40:41] op_sel:[1,0,0] op_sel_hi:[0,1,1]
	v_pk_fma_f32 v[2:3], v[2:3], v[82:83], v[46:47] op_sel_hi:[1,1,0]
	v_pk_fma_f32 v[4:5], v[4:5], v[84:85], v[48:49] op_sel_hi:[1,1,0]
	v_pk_mov_b32 v[42:43], v[52:53], v[50:51] op_sel:[1,0]
	v_mov_b32_e32 v53, v51
	v_and_b32_e32 v3, 0xffff0000, v49
	v_and_b32_e32 v5, 0xffff0000, v54
	v_pk_add_f32 v[30:31], v[30:31], v[32:33]
	v_pk_add_f32 v[32:33], v[34:35], v[36:37]
	v_pk_add_f32 v[36:37], v[42:43], v[52:53]
	v_pk_add_f32 v[34:35], v[38:39], v[40:41]
	v_or_b32_sdwa v39, v3, v29 dst_sel:DWORD dst_unused:UNUSED_PAD src0_sel:DWORD src1_sel:WORD_1
	v_or_b32_sdwa v38, v5, v47 dst_sel:DWORD dst_unused:UNUSED_PAD src0_sel:DWORD src1_sel:WORD_1
	v_mov_b32_e32 v3, v36
	v_mov_b32_e32 v5, v37
	v_pk_add_f32 v[2:3], v[2:3], v[4:5]
	v_pk_add_f32 v[26:27], v[26:27], v[30:31]
	v_pk_add_f32 v[24:25], v[24:25], v[32:33]
	v_pk_add_f32 v[18:19], v[18:19], v[34:35]
	global_store_dwordx2 v[22:23], v[38:39], off offset:512
	v_lshl_add_u64 v[22:23], v[22:23], 0, s[36:37]
	v_pk_add_f32 v[16:17], v[16:17], v[2:3]
	v_add_u32_e32 v29, s17, v28
	v_add_u32_e32 v90, s17, v1
	v_add_u32_e32 v98, 0x10000, v29
	v_add_u32_e32 v94, 0x12000, v29
	v_add_u32_e32 v102, 0x12400, v29
	ds_read_b128 v[30:33], v90
	ds_read_b128 v[34:37], v90 offset:1024
	ds_read_b128 v[38:41], v90 offset:8192
	ds_read_b128 v[42:45], v90 offset:9216
	ds_read_b128 v[46:49], v90 offset:16384
	ds_read_b128 v[50:53], v90 offset:17408
	ds_read_b128 v[54:57], v90 offset:24576
	ds_read_b128 v[58:61], v90 offset:25600
	ds_read_b128 v[62:65], v90 offset:32768
	ds_read_b128 v[66:69], v90 offset:33792
	ds_read_b128 v[70:73], v90 offset:40960
	ds_read_b128 v[74:77], v90 offset:41984
	ds_read_b128 v[78:81], v90 offset:49152
	ds_read_b128 v[82:85], v90 offset:50176
	ds_read_b128 v[86:89], v90 offset:57344
	ds_read_b128 v[90:93], v90 offset:58368
	v_add_u32_e32 v29, 0x10400, v29
	ds_read_b128 v[94:97], v94
	ds_read_b128 v[98:101], v98
	ds_read_b128 v[102:105], v102
	ds_read_b128 v[106:109], v29
	s_waitcnt lgkmcnt(14)
	v_pk_mov_b32 v[110:111], v[30:31], v[38:39] op_sel:[1,0]
	v_mov_b32_e32 v31, v39
	v_pk_mov_b32 v[38:39], v[32:33], v[40:41] op_sel:[1,0]
	v_mov_b32_e32 v33, v41
	s_waitcnt lgkmcnt(13)
	v_pk_mov_b32 v[40:41], v[46:47], v[54:55] op_sel:[1,0]
	v_mov_b32_e32 v47, v55
	v_pk_mov_b32 v[54:55], v[48:49], v[56:57] op_sel:[1,0]
	v_mov_b32_e32 v49, v57
	s_waitcnt lgkmcnt(9)
	v_pk_mov_b32 v[56:57], v[62:63], v[70:71] op_sel:[1,0]
	v_mov_b32_e32 v63, v71
	v_pk_mov_b32 v[70:71], v[64:65], v[72:73] op_sel:[1,0]
	v_mov_b32_e32 v65, v73
	v_pk_mov_b32 v[72:73], v[34:35], v[42:43] op_sel:[1,0]
	v_mov_b32_e32 v35, v43
	v_pk_mov_b32 v[42:43], v[36:37], v[44:45] op_sel:[1,0]
	v_mov_b32_e32 v37, v45
	v_pk_mov_b32 v[44:45], v[50:51], v[58:59] op_sel:[1,0]
	v_mov_b32_e32 v51, v59
	v_pk_mov_b32 v[58:59], v[52:53], v[60:61] op_sel:[1,0]
	v_mov_b32_e32 v53, v61
	s_waitcnt lgkmcnt(8)
	v_pk_mov_b32 v[60:61], v[66:67], v[74:75] op_sel:[1,0]
	v_mov_b32_e32 v67, v75
	v_pk_mov_b32 v[74:75], v[68:69], v[76:77] op_sel:[1,0]
	v_mov_b32_e32 v69, v77
	s_addk_i32 s17, 0x800
	s_waitcnt vmcnt(7) lgkmcnt(2)
	v_pk_fma_f32 v[96:97], v[122:123], v[96:97], v[100:101]
	v_pk_fma_f32 v[94:95], v[120:121], v[94:95], v[98:99]
	v_and_b32_sdwa v5, v97, v6 dst_sel:DWORD dst_unused:UNUSED_PAD src0_sel:WORD_1 src1_sel:DWORD
	v_and_b32_sdwa v3, v95, v6 dst_sel:DWORD dst_unused:UNUSED_PAD src0_sel:WORD_1 src1_sel:DWORD
	v_and_b32_sdwa v2, v94, v6 dst_sel:DWORD dst_unused:UNUSED_PAD src0_sel:WORD_1 src1_sel:DWORD
	v_and_b32_sdwa v4, v96, v6 dst_sel:DWORD dst_unused:UNUSED_PAD src0_sel:WORD_1 src1_sel:DWORD
	v_add3_u32 v3, v95, v3, s16
	v_add3_u32 v5, v97, v5, s16
	v_add3_u32 v2, v94, v2, s16
	v_add3_u32 v4, v96, v4, s16
	v_and_b32_e32 v5, 0xffff0000, v5
	v_and_b32_e32 v29, 0xffff0000, v3
	v_or_b32_sdwa v3, v5, v4 dst_sel:DWORD dst_unused:UNUSED_PAD src0_sel:DWORD src1_sel:WORD_1
	v_or_b32_sdwa v2, v29, v2 dst_sel:DWORD dst_unused:UNUSED_PAD src0_sel:DWORD src1_sel:WORD_1
	global_store_dwordx2 v[22:23], v[2:3], off
	v_pk_mul_f32 v[30:31], v[94:95], v[30:31]
	v_pk_mul_f32 v[32:33], v[96:97], v[32:33]
	v_pk_mul_f32 v[46:47], v[94:95], v[46:47]
	v_pk_mul_f32 v[48:49], v[96:97], v[48:49]
	v_pk_mul_f32 v[88:89], v[96:97], v[88:89]
	v_pk_mul_f32 v[86:87], v[94:95], v[86:87]
	v_mul_f32_e32 v76, v95, v79
	v_mul_f32_e32 v98, v97, v81
	v_pk_fma_f32 v[30:31], v[94:95], v[110:111], v[30:31] op_sel:[1,0,0] op_sel_hi:[0,1,1]
	v_pk_fma_f32 v[40:41], v[94:95], v[40:41], v[46:47] op_sel:[1,0,0] op_sel_hi:[0,1,1]
	v_pk_fma_f32 v[32:33], v[96:97], v[38:39], v[32:33] op_sel:[1,0,0] op_sel_hi:[0,1,1]
	v_pk_fma_f32 v[38:39], v[96:97], v[54:55], v[48:49] op_sel:[1,0,0] op_sel_hi:[0,1,1]
	v_pk_mov_b32 v[54:55], v[86:87], v[88:89] op_sel:[1,0]
	v_mov_b32_e32 v87, v89
	v_pk_mul_f32 v[62:63], v[94:95], v[62:63]
	v_pk_mul_f32 v[64:65], v[96:97], v[64:65]
	v_pk_fma_f32 v[76:77], v[94:95], v[78:79], v[76:77] op_sel_hi:[1,1,0]
	v_pk_fma_f32 v[78:79], v[96:97], v[80:81], v[98:99] op_sel_hi:[1,1,0]
	v_pk_add_f32 v[30:31], v[30:31], v[32:33]
	v_pk_add_f32 v[32:33], v[40:41], v[38:39]
	v_pk_add_f32 v[40:41], v[54:55], v[86:87]
	v_pk_fma_f32 v[46:47], v[94:95], v[56:57], v[62:63] op_sel:[1,0,0] op_sel_hi:[0,1,1]
	v_pk_fma_f32 v[48:49], v[96:97], v[70:71], v[64:65] op_sel:[1,0,0] op_sel_hi:[0,1,1]
	v_mov_b32_e32 v77, v40
	v_mov_b32_e32 v79, v41
	v_pk_add_f32 v[38:39], v[46:47], v[48:49]
	v_pk_add_f32 v[26:27], v[26:27], v[30:31]
	v_pk_add_f32 v[30:31], v[76:77], v[78:79]
	v_pk_add_f32 v[24:25], v[24:25], v[32:33]
	v_pk_add_f32 v[18:19], v[18:19], v[38:39]
	v_pk_add_f32 v[16:17], v[16:17], v[30:31]
	v_lshl_add_u64 v[20:21], v[20:21], 0, s[40:41]
	s_waitcnt vmcnt(7) lgkmcnt(0)
	v_pk_fma_f32 v[4:5], v[126:127], v[104:105], v[108:109]
	v_pk_fma_f32 v[2:3], v[124:125], v[102:103], v[106:107]
	v_and_b32_sdwa v49, v5, v6 dst_sel:DWORD dst_unused:UNUSED_PAD src0_sel:WORD_1 src1_sel:DWORD
	v_and_b32_sdwa v47, v2, v6 dst_sel:DWORD dst_unused:UNUSED_PAD src0_sel:WORD_1 src1_sel:DWORD
	v_and_b32_sdwa v29, v4, v6 dst_sel:DWORD dst_unused:UNUSED_PAD src0_sel:WORD_1 src1_sel:DWORD
	v_and_b32_sdwa v54, v3, v6 dst_sel:DWORD dst_unused:UNUSED_PAD src0_sel:WORD_1 src1_sel:DWORD
	v_pk_mul_f32 v[30:31], v[2:3], v[34:35]
	v_pk_mul_f32 v[32:33], v[4:5], v[36:37]
	v_pk_mul_f32 v[34:35], v[2:3], v[50:51]
	v_pk_mul_f32 v[36:37], v[4:5], v[52:53]
	v_pk_mul_f32 v[38:39], v[2:3], v[66:67]
	v_pk_mul_f32 v[40:41], v[4:5], v[68:69]
	v_mul_f32_e32 v46, v3, v83
	v_mul_f32_e32 v48, v5, v85
	v_pk_mul_f32 v[50:51], v[4:5], v[92:93]
	v_pk_mul_f32 v[52:53], v[2:3], v[90:91]
	v_add3_u32 v47, v2, v47, s16
	v_add3_u32 v49, v5, v49, s16
	v_add3_u32 v29, v4, v29, s16
	v_add3_u32 v54, v3, v54, s16
	v_pk_fma_f32 v[30:31], v[2:3], v[72:73], v[30:31] op_sel:[1,0,0] op_sel_hi:[0,1,1]
	v_pk_fma_f32 v[32:33], v[4:5], v[42:43], v[32:33] op_sel:[1,0,0] op_sel_hi:[0,1,1]
	v_pk_fma_f32 v[34:35], v[2:3], v[44:45], v[34:35] op_sel:[1,0,0] op_sel_hi:[0,1,1]
	v_pk_fma_f32 v[36:37], v[4:5], v[58:59], v[36:37] op_sel:[1,0,0] op_sel_hi:[0,1,1]
	v_pk_fma_f32 v[38:39], v[2:3], v[60:61], v[38:39] op_sel:[1,0,0] op_sel_hi:[0,1,1]
	v_pk_fma_f32 v[40:41], v[4:5], v[74:75], v[40:41] op_sel:[1,0,0] op_sel_hi:[0,1,1]
	v_pk_fma_f32 v[2:3], v[2:3], v[82:83], v[46:47] op_sel_hi:[1,1,0]
	v_pk_fma_f32 v[4:5], v[4:5], v[84:85], v[48:49] op_sel_hi:[1,1,0]
	v_pk_mov_b32 v[42:43], v[52:53], v[50:51] op_sel:[1,0]
	v_mov_b32_e32 v53, v51
	v_and_b32_e32 v3, 0xffff0000, v49
	v_and_b32_e32 v5, 0xffff0000, v54
	v_pk_add_f32 v[30:31], v[30:31], v[32:33]
	v_pk_add_f32 v[32:33], v[34:35], v[36:37]
	v_pk_add_f32 v[36:37], v[42:43], v[52:53]
	v_pk_add_f32 v[34:35], v[38:39], v[40:41]
	v_or_b32_sdwa v39, v3, v29 dst_sel:DWORD dst_unused:UNUSED_PAD src0_sel:DWORD src1_sel:WORD_1
	v_or_b32_sdwa v38, v5, v47 dst_sel:DWORD dst_unused:UNUSED_PAD src0_sel:DWORD src1_sel:WORD_1
	v_mov_b32_e32 v3, v36
	v_mov_b32_e32 v5, v37
	v_pk_add_f32 v[2:3], v[2:3], v[4:5]
	v_pk_add_f32 v[26:27], v[26:27], v[30:31]
	v_pk_add_f32 v[24:25], v[24:25], v[32:33]
	v_pk_add_f32 v[18:19], v[18:19], v[34:35]
	global_store_dwordx2 v[22:23], v[38:39], off offset:512
	v_lshl_add_u64 v[22:23], v[22:23], 0, s[36:37]
	v_pk_add_f32 v[16:17], v[16:17], v[2:3]
	v_add_u32_e32 v29, s17, v28
	v_add_u32_e32 v90, s17, v1
	v_add_u32_e32 v98, 0x10000, v29
	v_add_u32_e32 v94, 0x12000, v29
	v_add_u32_e32 v102, 0x12400, v29
	ds_read_b128 v[30:33], v90
	ds_read_b128 v[34:37], v90 offset:1024
	ds_read_b128 v[38:41], v90 offset:8192
	ds_read_b128 v[42:45], v90 offset:9216
	ds_read_b128 v[46:49], v90 offset:16384
	ds_read_b128 v[50:53], v90 offset:17408
	ds_read_b128 v[54:57], v90 offset:24576
	ds_read_b128 v[58:61], v90 offset:25600
	ds_read_b128 v[62:65], v90 offset:32768
	ds_read_b128 v[66:69], v90 offset:33792
	ds_read_b128 v[70:73], v90 offset:40960
	ds_read_b128 v[74:77], v90 offset:41984
	ds_read_b128 v[78:81], v90 offset:49152
	ds_read_b128 v[82:85], v90 offset:50176
	ds_read_b128 v[86:89], v90 offset:57344
	ds_read_b128 v[90:93], v90 offset:58368
	v_add_u32_e32 v29, 0x10400, v29
	ds_read_b128 v[94:97], v94
	ds_read_b128 v[98:101], v98
	ds_read_b128 v[102:105], v102
	ds_read_b128 v[106:109], v29
	s_waitcnt lgkmcnt(14)
	v_pk_mov_b32 v[110:111], v[30:31], v[38:39] op_sel:[1,0]
	v_mov_b32_e32 v31, v39
	v_pk_mov_b32 v[38:39], v[32:33], v[40:41] op_sel:[1,0]
	v_mov_b32_e32 v33, v41
	s_waitcnt lgkmcnt(13)
	v_pk_mov_b32 v[40:41], v[46:47], v[54:55] op_sel:[1,0]
	v_mov_b32_e32 v47, v55
	v_pk_mov_b32 v[54:55], v[48:49], v[56:57] op_sel:[1,0]
	v_mov_b32_e32 v49, v57
	s_waitcnt lgkmcnt(9)
	v_pk_mov_b32 v[56:57], v[62:63], v[70:71] op_sel:[1,0]
	v_mov_b32_e32 v63, v71
	v_pk_mov_b32 v[70:71], v[64:65], v[72:73] op_sel:[1,0]
	v_mov_b32_e32 v65, v73
	v_pk_mov_b32 v[72:73], v[34:35], v[42:43] op_sel:[1,0]
	v_mov_b32_e32 v35, v43
	v_pk_mov_b32 v[42:43], v[36:37], v[44:45] op_sel:[1,0]
	v_mov_b32_e32 v37, v45
	v_pk_mov_b32 v[44:45], v[50:51], v[58:59] op_sel:[1,0]
	v_mov_b32_e32 v51, v59
	v_pk_mov_b32 v[58:59], v[52:53], v[60:61] op_sel:[1,0]
	v_mov_b32_e32 v53, v61
	s_waitcnt lgkmcnt(8)
	v_pk_mov_b32 v[60:61], v[66:67], v[74:75] op_sel:[1,0]
	v_mov_b32_e32 v67, v75
	v_pk_mov_b32 v[74:75], v[68:69], v[76:77] op_sel:[1,0]
	v_mov_b32_e32 v69, v77
	s_addk_i32 s17, 0x800
	s_waitcnt vmcnt(7) lgkmcnt(2)
	v_pk_fma_f32 v[96:97], v[130:131], v[96:97], v[100:101]
	v_pk_fma_f32 v[94:95], v[128:129], v[94:95], v[98:99]
	v_and_b32_sdwa v5, v97, v6 dst_sel:DWORD dst_unused:UNUSED_PAD src0_sel:WORD_1 src1_sel:DWORD
	v_and_b32_sdwa v3, v95, v6 dst_sel:DWORD dst_unused:UNUSED_PAD src0_sel:WORD_1 src1_sel:DWORD
	v_and_b32_sdwa v2, v94, v6 dst_sel:DWORD dst_unused:UNUSED_PAD src0_sel:WORD_1 src1_sel:DWORD
	v_and_b32_sdwa v4, v96, v6 dst_sel:DWORD dst_unused:UNUSED_PAD src0_sel:WORD_1 src1_sel:DWORD
	v_add3_u32 v3, v95, v3, s16
	v_add3_u32 v5, v97, v5, s16
	v_add3_u32 v2, v94, v2, s16
	v_add3_u32 v4, v96, v4, s16
	v_and_b32_e32 v5, 0xffff0000, v5
	v_and_b32_e32 v29, 0xffff0000, v3
	v_or_b32_sdwa v3, v5, v4 dst_sel:DWORD dst_unused:UNUSED_PAD src0_sel:DWORD src1_sel:WORD_1
	v_or_b32_sdwa v2, v29, v2 dst_sel:DWORD dst_unused:UNUSED_PAD src0_sel:DWORD src1_sel:WORD_1
	global_store_dwordx2 v[22:23], v[2:3], off
	v_pk_mul_f32 v[30:31], v[94:95], v[30:31]
	v_pk_mul_f32 v[32:33], v[96:97], v[32:33]
	v_pk_mul_f32 v[46:47], v[94:95], v[46:47]
	v_pk_mul_f32 v[48:49], v[96:97], v[48:49]
	v_pk_mul_f32 v[88:89], v[96:97], v[88:89]
	v_pk_mul_f32 v[86:87], v[94:95], v[86:87]
	v_mul_f32_e32 v76, v95, v79
	v_mul_f32_e32 v98, v97, v81
	v_pk_fma_f32 v[30:31], v[94:95], v[110:111], v[30:31] op_sel:[1,0,0] op_sel_hi:[0,1,1]
	v_pk_fma_f32 v[40:41], v[94:95], v[40:41], v[46:47] op_sel:[1,0,0] op_sel_hi:[0,1,1]
	v_pk_fma_f32 v[32:33], v[96:97], v[38:39], v[32:33] op_sel:[1,0,0] op_sel_hi:[0,1,1]
	v_pk_fma_f32 v[38:39], v[96:97], v[54:55], v[48:49] op_sel:[1,0,0] op_sel_hi:[0,1,1]
	v_pk_mov_b32 v[54:55], v[86:87], v[88:89] op_sel:[1,0]
	v_mov_b32_e32 v87, v89
	v_pk_mul_f32 v[62:63], v[94:95], v[62:63]
	v_pk_mul_f32 v[64:65], v[96:97], v[64:65]
	v_pk_fma_f32 v[76:77], v[94:95], v[78:79], v[76:77] op_sel_hi:[1,1,0]
	v_pk_fma_f32 v[78:79], v[96:97], v[80:81], v[98:99] op_sel_hi:[1,1,0]
	v_pk_add_f32 v[30:31], v[30:31], v[32:33]
	v_pk_add_f32 v[32:33], v[40:41], v[38:39]
	v_pk_add_f32 v[40:41], v[54:55], v[86:87]
	v_pk_fma_f32 v[46:47], v[94:95], v[56:57], v[62:63] op_sel:[1,0,0] op_sel_hi:[0,1,1]
	v_pk_fma_f32 v[48:49], v[96:97], v[70:71], v[64:65] op_sel:[1,0,0] op_sel_hi:[0,1,1]
	v_mov_b32_e32 v77, v40
	v_mov_b32_e32 v79, v41
	v_pk_add_f32 v[38:39], v[46:47], v[48:49]
	v_pk_add_f32 v[26:27], v[26:27], v[30:31]
	v_pk_add_f32 v[30:31], v[76:77], v[78:79]
	v_pk_add_f32 v[24:25], v[24:25], v[32:33]
	v_pk_add_f32 v[18:19], v[18:19], v[38:39]
	v_pk_add_f32 v[16:17], v[16:17], v[30:31]
	v_lshl_add_u64 v[20:21], v[20:21], 0, s[40:41]
	s_waitcnt vmcnt(7) lgkmcnt(0)
	v_pk_fma_f32 v[4:5], v[134:135], v[104:105], v[108:109]
	v_pk_fma_f32 v[2:3], v[132:133], v[102:103], v[106:107]
	v_and_b32_sdwa v49, v5, v6 dst_sel:DWORD dst_unused:UNUSED_PAD src0_sel:WORD_1 src1_sel:DWORD
	v_and_b32_sdwa v47, v2, v6 dst_sel:DWORD dst_unused:UNUSED_PAD src0_sel:WORD_1 src1_sel:DWORD
	v_and_b32_sdwa v29, v4, v6 dst_sel:DWORD dst_unused:UNUSED_PAD src0_sel:WORD_1 src1_sel:DWORD
	v_and_b32_sdwa v54, v3, v6 dst_sel:DWORD dst_unused:UNUSED_PAD src0_sel:WORD_1 src1_sel:DWORD
	v_pk_mul_f32 v[30:31], v[2:3], v[34:35]
	v_pk_mul_f32 v[32:33], v[4:5], v[36:37]
	v_pk_mul_f32 v[34:35], v[2:3], v[50:51]
	v_pk_mul_f32 v[36:37], v[4:5], v[52:53]
	v_pk_mul_f32 v[38:39], v[2:3], v[66:67]
	v_pk_mul_f32 v[40:41], v[4:5], v[68:69]
	v_mul_f32_e32 v46, v3, v83
	v_mul_f32_e32 v48, v5, v85
	v_pk_mul_f32 v[50:51], v[4:5], v[92:93]
	v_pk_mul_f32 v[52:53], v[2:3], v[90:91]
	v_add3_u32 v47, v2, v47, s16
	v_add3_u32 v49, v5, v49, s16
	v_add3_u32 v29, v4, v29, s16
	v_add3_u32 v54, v3, v54, s16
	v_pk_fma_f32 v[30:31], v[2:3], v[72:73], v[30:31] op_sel:[1,0,0] op_sel_hi:[0,1,1]
	v_pk_fma_f32 v[32:33], v[4:5], v[42:43], v[32:33] op_sel:[1,0,0] op_sel_hi:[0,1,1]
	v_pk_fma_f32 v[34:35], v[2:3], v[44:45], v[34:35] op_sel:[1,0,0] op_sel_hi:[0,1,1]
	v_pk_fma_f32 v[36:37], v[4:5], v[58:59], v[36:37] op_sel:[1,0,0] op_sel_hi:[0,1,1]
	v_pk_fma_f32 v[38:39], v[2:3], v[60:61], v[38:39] op_sel:[1,0,0] op_sel_hi:[0,1,1]
	v_pk_fma_f32 v[40:41], v[4:5], v[74:75], v[40:41] op_sel:[1,0,0] op_sel_hi:[0,1,1]
	v_pk_fma_f32 v[2:3], v[2:3], v[82:83], v[46:47] op_sel_hi:[1,1,0]
	v_pk_fma_f32 v[4:5], v[4:5], v[84:85], v[48:49] op_sel_hi:[1,1,0]
	v_pk_mov_b32 v[42:43], v[52:53], v[50:51] op_sel:[1,0]
	v_mov_b32_e32 v53, v51
	v_and_b32_e32 v3, 0xffff0000, v49
	v_and_b32_e32 v5, 0xffff0000, v54
	v_pk_add_f32 v[30:31], v[30:31], v[32:33]
	v_pk_add_f32 v[32:33], v[34:35], v[36:37]
	v_pk_add_f32 v[36:37], v[42:43], v[52:53]
	v_pk_add_f32 v[34:35], v[38:39], v[40:41]
	v_or_b32_sdwa v39, v3, v29 dst_sel:DWORD dst_unused:UNUSED_PAD src0_sel:DWORD src1_sel:WORD_1
	v_or_b32_sdwa v38, v5, v47 dst_sel:DWORD dst_unused:UNUSED_PAD src0_sel:DWORD src1_sel:WORD_1
	v_mov_b32_e32 v3, v36
	v_mov_b32_e32 v5, v37
	v_pk_add_f32 v[2:3], v[2:3], v[4:5]
	v_pk_add_f32 v[26:27], v[26:27], v[30:31]
	v_pk_add_f32 v[24:25], v[24:25], v[32:33]
	v_pk_add_f32 v[18:19], v[18:19], v[34:35]
	global_store_dwordx2 v[22:23], v[38:39], off offset:512
	v_lshl_add_u64 v[22:23], v[22:23], 0, s[36:37]
	v_pk_add_f32 v[16:17], v[16:17], v[2:3]
	v_add_u32_e32 v29, s17, v28
	v_add_u32_e32 v90, s17, v1
	v_add_u32_e32 v98, 0x10000, v29
	v_add_u32_e32 v94, 0x12000, v29
	v_add_u32_e32 v102, 0x12400, v29
	ds_read_b128 v[30:33], v90
	ds_read_b128 v[34:37], v90 offset:1024
	ds_read_b128 v[38:41], v90 offset:8192
	ds_read_b128 v[42:45], v90 offset:9216
	ds_read_b128 v[46:49], v90 offset:16384
	ds_read_b128 v[50:53], v90 offset:17408
	ds_read_b128 v[54:57], v90 offset:24576
	ds_read_b128 v[58:61], v90 offset:25600
	ds_read_b128 v[62:65], v90 offset:32768
	ds_read_b128 v[66:69], v90 offset:33792
	ds_read_b128 v[70:73], v90 offset:40960
	ds_read_b128 v[74:77], v90 offset:41984
	ds_read_b128 v[78:81], v90 offset:49152
	ds_read_b128 v[82:85], v90 offset:50176
	ds_read_b128 v[86:89], v90 offset:57344
	ds_read_b128 v[90:93], v90 offset:58368
	v_add_u32_e32 v29, 0x10400, v29
	ds_read_b128 v[94:97], v94
	ds_read_b128 v[98:101], v98
	ds_read_b128 v[102:105], v102
	ds_read_b128 v[106:109], v29
	s_waitcnt lgkmcnt(14)
	v_pk_mov_b32 v[110:111], v[30:31], v[38:39] op_sel:[1,0]
	v_mov_b32_e32 v31, v39
	v_pk_mov_b32 v[38:39], v[32:33], v[40:41] op_sel:[1,0]
	v_mov_b32_e32 v33, v41
	s_waitcnt lgkmcnt(13)
	v_pk_mov_b32 v[40:41], v[46:47], v[54:55] op_sel:[1,0]
	v_mov_b32_e32 v47, v55
	v_pk_mov_b32 v[54:55], v[48:49], v[56:57] op_sel:[1,0]
	v_mov_b32_e32 v49, v57
	s_waitcnt lgkmcnt(9)
	v_pk_mov_b32 v[56:57], v[62:63], v[70:71] op_sel:[1,0]
	v_mov_b32_e32 v63, v71
	v_pk_mov_b32 v[70:71], v[64:65], v[72:73] op_sel:[1,0]
	v_mov_b32_e32 v65, v73
	v_pk_mov_b32 v[72:73], v[34:35], v[42:43] op_sel:[1,0]
	v_mov_b32_e32 v35, v43
	v_pk_mov_b32 v[42:43], v[36:37], v[44:45] op_sel:[1,0]
	v_mov_b32_e32 v37, v45
	v_pk_mov_b32 v[44:45], v[50:51], v[58:59] op_sel:[1,0]
	v_mov_b32_e32 v51, v59
	v_pk_mov_b32 v[58:59], v[52:53], v[60:61] op_sel:[1,0]
	v_mov_b32_e32 v53, v61
	s_waitcnt lgkmcnt(8)
	v_pk_mov_b32 v[60:61], v[66:67], v[74:75] op_sel:[1,0]
	v_mov_b32_e32 v67, v75
	v_pk_mov_b32 v[74:75], v[68:69], v[76:77] op_sel:[1,0]
	v_mov_b32_e32 v69, v77
	s_addk_i32 s17, 0x800
	s_waitcnt vmcnt(7) lgkmcnt(2)
	v_pk_fma_f32 v[96:97], v[138:139], v[96:97], v[100:101]
	v_pk_fma_f32 v[94:95], v[136:137], v[94:95], v[98:99]
	v_and_b32_sdwa v5, v97, v6 dst_sel:DWORD dst_unused:UNUSED_PAD src0_sel:WORD_1 src1_sel:DWORD
	v_and_b32_sdwa v3, v95, v6 dst_sel:DWORD dst_unused:UNUSED_PAD src0_sel:WORD_1 src1_sel:DWORD
	v_and_b32_sdwa v2, v94, v6 dst_sel:DWORD dst_unused:UNUSED_PAD src0_sel:WORD_1 src1_sel:DWORD
	v_and_b32_sdwa v4, v96, v6 dst_sel:DWORD dst_unused:UNUSED_PAD src0_sel:WORD_1 src1_sel:DWORD
	v_add3_u32 v3, v95, v3, s16
	v_add3_u32 v5, v97, v5, s16
	v_add3_u32 v2, v94, v2, s16
	v_add3_u32 v4, v96, v4, s16
	v_and_b32_e32 v5, 0xffff0000, v5
	v_and_b32_e32 v29, 0xffff0000, v3
	v_or_b32_sdwa v3, v5, v4 dst_sel:DWORD dst_unused:UNUSED_PAD src0_sel:DWORD src1_sel:WORD_1
	v_or_b32_sdwa v2, v29, v2 dst_sel:DWORD dst_unused:UNUSED_PAD src0_sel:DWORD src1_sel:WORD_1
	global_store_dwordx2 v[22:23], v[2:3], off
	v_pk_mul_f32 v[30:31], v[94:95], v[30:31]
	v_pk_mul_f32 v[32:33], v[96:97], v[32:33]
	v_pk_mul_f32 v[46:47], v[94:95], v[46:47]
	v_pk_mul_f32 v[48:49], v[96:97], v[48:49]
	v_pk_mul_f32 v[88:89], v[96:97], v[88:89]
	v_pk_mul_f32 v[86:87], v[94:95], v[86:87]
	v_mul_f32_e32 v76, v95, v79
	v_mul_f32_e32 v98, v97, v81
	v_pk_fma_f32 v[30:31], v[94:95], v[110:111], v[30:31] op_sel:[1,0,0] op_sel_hi:[0,1,1]
	v_pk_fma_f32 v[40:41], v[94:95], v[40:41], v[46:47] op_sel:[1,0,0] op_sel_hi:[0,1,1]
	v_pk_fma_f32 v[32:33], v[96:97], v[38:39], v[32:33] op_sel:[1,0,0] op_sel_hi:[0,1,1]
	v_pk_fma_f32 v[38:39], v[96:97], v[54:55], v[48:49] op_sel:[1,0,0] op_sel_hi:[0,1,1]
	v_pk_mov_b32 v[54:55], v[86:87], v[88:89] op_sel:[1,0]
	v_mov_b32_e32 v87, v89
	v_pk_mul_f32 v[62:63], v[94:95], v[62:63]
	v_pk_mul_f32 v[64:65], v[96:97], v[64:65]
	v_pk_fma_f32 v[76:77], v[94:95], v[78:79], v[76:77] op_sel_hi:[1,1,0]
	v_pk_fma_f32 v[78:79], v[96:97], v[80:81], v[98:99] op_sel_hi:[1,1,0]
	v_pk_add_f32 v[30:31], v[30:31], v[32:33]
	v_pk_add_f32 v[32:33], v[40:41], v[38:39]
	v_pk_add_f32 v[40:41], v[54:55], v[86:87]
	v_pk_fma_f32 v[46:47], v[94:95], v[56:57], v[62:63] op_sel:[1,0,0] op_sel_hi:[0,1,1]
	v_pk_fma_f32 v[48:49], v[96:97], v[70:71], v[64:65] op_sel:[1,0,0] op_sel_hi:[0,1,1]
	v_mov_b32_e32 v77, v40
	v_mov_b32_e32 v79, v41
	v_pk_add_f32 v[38:39], v[46:47], v[48:49]
	v_pk_add_f32 v[26:27], v[26:27], v[30:31]
	v_pk_add_f32 v[30:31], v[76:77], v[78:79]
	v_pk_add_f32 v[24:25], v[24:25], v[32:33]
	v_pk_add_f32 v[18:19], v[18:19], v[38:39]
	v_pk_add_f32 v[16:17], v[16:17], v[30:31]
	v_lshl_add_u64 v[20:21], v[20:21], 0, s[40:41]
	s_waitcnt vmcnt(7) lgkmcnt(0)
	v_pk_fma_f32 v[4:5], v[142:143], v[104:105], v[108:109]
	v_pk_fma_f32 v[2:3], v[140:141], v[102:103], v[106:107]
	v_and_b32_sdwa v49, v5, v6 dst_sel:DWORD dst_unused:UNUSED_PAD src0_sel:WORD_1 src1_sel:DWORD
	v_and_b32_sdwa v47, v2, v6 dst_sel:DWORD dst_unused:UNUSED_PAD src0_sel:WORD_1 src1_sel:DWORD
	v_and_b32_sdwa v29, v4, v6 dst_sel:DWORD dst_unused:UNUSED_PAD src0_sel:WORD_1 src1_sel:DWORD
	v_and_b32_sdwa v54, v3, v6 dst_sel:DWORD dst_unused:UNUSED_PAD src0_sel:WORD_1 src1_sel:DWORD
	v_pk_mul_f32 v[30:31], v[2:3], v[34:35]
	v_pk_mul_f32 v[32:33], v[4:5], v[36:37]
	v_pk_mul_f32 v[34:35], v[2:3], v[50:51]
	v_pk_mul_f32 v[36:37], v[4:5], v[52:53]
	v_pk_mul_f32 v[38:39], v[2:3], v[66:67]
	v_pk_mul_f32 v[40:41], v[4:5], v[68:69]
	v_mul_f32_e32 v46, v3, v83
	v_mul_f32_e32 v48, v5, v85
	v_pk_mul_f32 v[50:51], v[4:5], v[92:93]
	v_pk_mul_f32 v[52:53], v[2:3], v[90:91]
	v_add3_u32 v47, v2, v47, s16
	v_add3_u32 v49, v5, v49, s16
	v_add3_u32 v29, v4, v29, s16
	v_add3_u32 v54, v3, v54, s16
	v_pk_fma_f32 v[30:31], v[2:3], v[72:73], v[30:31] op_sel:[1,0,0] op_sel_hi:[0,1,1]
	v_pk_fma_f32 v[32:33], v[4:5], v[42:43], v[32:33] op_sel:[1,0,0] op_sel_hi:[0,1,1]
	v_pk_fma_f32 v[34:35], v[2:3], v[44:45], v[34:35] op_sel:[1,0,0] op_sel_hi:[0,1,1]
	v_pk_fma_f32 v[36:37], v[4:5], v[58:59], v[36:37] op_sel:[1,0,0] op_sel_hi:[0,1,1]
	v_pk_fma_f32 v[38:39], v[2:3], v[60:61], v[38:39] op_sel:[1,0,0] op_sel_hi:[0,1,1]
	v_pk_fma_f32 v[40:41], v[4:5], v[74:75], v[40:41] op_sel:[1,0,0] op_sel_hi:[0,1,1]
	v_pk_fma_f32 v[2:3], v[2:3], v[82:83], v[46:47] op_sel_hi:[1,1,0]
	v_pk_fma_f32 v[4:5], v[4:5], v[84:85], v[48:49] op_sel_hi:[1,1,0]
	v_pk_mov_b32 v[42:43], v[52:53], v[50:51] op_sel:[1,0]
	v_mov_b32_e32 v53, v51
	v_and_b32_e32 v3, 0xffff0000, v49
	v_and_b32_e32 v5, 0xffff0000, v54
	v_pk_add_f32 v[30:31], v[30:31], v[32:33]
	v_pk_add_f32 v[32:33], v[34:35], v[36:37]
	v_pk_add_f32 v[36:37], v[42:43], v[52:53]
	v_pk_add_f32 v[34:35], v[38:39], v[40:41]
	v_or_b32_sdwa v39, v3, v29 dst_sel:DWORD dst_unused:UNUSED_PAD src0_sel:DWORD src1_sel:WORD_1
	v_or_b32_sdwa v38, v5, v47 dst_sel:DWORD dst_unused:UNUSED_PAD src0_sel:DWORD src1_sel:WORD_1
	v_mov_b32_e32 v3, v36
	v_mov_b32_e32 v5, v37
	v_pk_add_f32 v[2:3], v[2:3], v[4:5]
	v_pk_add_f32 v[26:27], v[26:27], v[30:31]
	v_pk_add_f32 v[24:25], v[24:25], v[32:33]
	v_pk_add_f32 v[18:19], v[18:19], v[34:35]
	global_store_dwordx2 v[22:23], v[38:39], off offset:512
	v_lshl_add_u64 v[22:23], v[22:23], 0, s[36:37]
	v_pk_add_f32 v[16:17], v[16:17], v[2:3]
	v_add_f32_dpp v2, v26, v26 quad_perm:[1,0,3,2] row_mask:0xf bank_mask:0xf bound_ctrl:1
	v_add_f32_dpp v4, v27, v27 quad_perm:[1,0,3,2] row_mask:0xf bank_mask:0xf bound_ctrl:1
	v_add_f32_dpp v20, v24, v24 quad_perm:[1,0,3,2] row_mask:0xf bank_mask:0xf bound_ctrl:1
	v_add_f32_dpp v2, v2, v2 quad_perm:[2,3,0,1] row_mask:0xf bank_mask:0xf bound_ctrl:1
	v_add_f32_dpp v4, v4, v4 quad_perm:[2,3,0,1] row_mask:0xf bank_mask:0xf bound_ctrl:1
	v_add_f32_dpp v20, v20, v20 quad_perm:[2,3,0,1] row_mask:0xf bank_mask:0xf bound_ctrl:1
	v_add_f32_dpp v2, v2, v2 row_half_mirror row_mask:0xf bank_mask:0xf bound_ctrl:1
	v_add_f32_dpp v4, v4, v4 row_half_mirror row_mask:0xf bank_mask:0xf bound_ctrl:1
	v_add_f32_dpp v20, v20, v20 row_half_mirror row_mask:0xf bank_mask:0xf bound_ctrl:1
	v_add_f32_dpp v2, v2, v2 row_mirror row_mask:0xf bank_mask:0xf bound_ctrl:1
	v_mov_b32_e32 v3, v2
	v_add_f32_dpp v4, v4, v4 row_mirror row_mask:0xf bank_mask:0xf bound_ctrl:1
	s_nop 0
	v_permlane16_swap_b32_e32 v2, v3
	v_add_f32_e32 v2, v2, v3
	v_mov_b32_e32 v3, v2
	v_mov_b32_e32 v5, v4
	v_add_f32_dpp v20, v20, v20 row_mirror row_mask:0xf bank_mask:0xf bound_ctrl:1
	s_nop 0
	v_permlane16_swap_b32_e32 v4, v5
	v_add_f32_e32 v4, v4, v5
	v_mov_b32_e32 v5, v4
	v_mov_b32_e32 v21, v20
	v_add_f32_dpp v22, v25, v25 quad_perm:[1,0,3,2] row_mask:0xf bank_mask:0xf bound_ctrl:1
	v_add_f32_dpp v18, v18, v18 quad_perm:[1,0,3,2] row_mask:0xf bank_mask:0xf bound_ctrl:1
	v_permlane16_swap_b32_e32 v20, v21
	v_add_f32_dpp v22, v22, v22 quad_perm:[2,3,0,1] row_mask:0xf bank_mask:0xf bound_ctrl:1
	v_add_f32_e32 v20, v20, v21
	v_mov_b32_e32 v21, v20
	v_add_f32_dpp v22, v22, v22 row_half_mirror row_mask:0xf bank_mask:0xf bound_ctrl:1
	v_add_f32_dpp v18, v18, v18 quad_perm:[2,3,0,1] row_mask:0xf bank_mask:0xf bound_ctrl:1
	v_add_f32_dpp v19, v19, v19 quad_perm:[1,0,3,2] row_mask:0xf bank_mask:0xf bound_ctrl:1
	v_add_f32_dpp v22, v22, v22 row_mirror row_mask:0xf bank_mask:0xf bound_ctrl:1
	v_mov_b32_e32 v23, v22
	v_add_f32_dpp v18, v18, v18 row_half_mirror row_mask:0xf bank_mask:0xf bound_ctrl:1
	s_nop 0
	v_permlane16_swap_b32_e32 v22, v23
	v_add_f32_e32 v22, v22, v23
	v_add_f32_dpp v18, v18, v18 row_mirror row_mask:0xf bank_mask:0xf bound_ctrl:1
	v_mov_b32_e32 v23, v22
	v_mov_b32_e32 v24, v18
	v_add_f32_dpp v19, v19, v19 quad_perm:[2,3,0,1] row_mask:0xf bank_mask:0xf bound_ctrl:1
	s_nop 0
	v_permlane16_swap_b32_e32 v18, v24
	v_add_f32_dpp v19, v19, v19 row_half_mirror row_mask:0xf bank_mask:0xf bound_ctrl:1
	v_add_f32_e32 v18, v18, v24
	v_mov_b32_e32 v24, v18
	v_add_f32_dpp v19, v19, v19 row_mirror row_mask:0xf bank_mask:0xf bound_ctrl:1
	v_mov_b32_e32 v25, v19
	v_add_f32_dpp v16, v16, v16 quad_perm:[1,0,3,2] row_mask:0xf bank_mask:0xf bound_ctrl:1
	v_add_f32_dpp v17, v17, v17 quad_perm:[1,0,3,2] row_mask:0xf bank_mask:0xf bound_ctrl:1
	v_permlane16_swap_b32_e32 v19, v25
	v_add_f32_dpp v16, v16, v16 quad_perm:[2,3,0,1] row_mask:0xf bank_mask:0xf bound_ctrl:1
	v_add_f32_e32 v19, v19, v25
	v_mov_b32_e32 v25, v19
	v_add_f32_dpp v16, v16, v16 row_half_mirror row_mask:0xf bank_mask:0xf bound_ctrl:1
	v_add_f32_dpp v17, v17, v17 quad_perm:[2,3,0,1] row_mask:0xf bank_mask:0xf bound_ctrl:1
	v_permlane32_swap_b32_e32 v2, v3
	v_add_f32_dpp v16, v16, v16 row_mirror row_mask:0xf bank_mask:0xf bound_ctrl:1
	v_mov_b32_e32 v26, v16
	v_add_f32_dpp v17, v17, v17 row_half_mirror row_mask:0xf bank_mask:0xf bound_ctrl:1
	s_nop 0
	v_permlane16_swap_b32_e32 v16, v26
	v_add_f32_e32 v16, v16, v26
	v_add_f32_dpp v17, v17, v17 row_mirror row_mask:0xf bank_mask:0xf bound_ctrl:1
	v_mov_b32_e32 v26, v16
	v_mov_b32_e32 v27, v17
	v_permlane32_swap_b32_e32 v4, v5
	s_nop 0
	v_permlane16_swap_b32_e32 v17, v27
	v_add_f32_e32 v17, v17, v27
	v_mov_b32_e32 v27, v17
	v_permlane32_swap_b32_e32 v20, v21
	v_permlane32_swap_b32_e32 v22, v23
	v_permlane32_swap_b32_e32 v18, v24
	v_permlane32_swap_b32_e32 v19, v25
	v_permlane32_swap_b32_e32 v16, v26
	v_permlane32_swap_b32_e32 v17, v27
	s_and_saveexec_b64 s[42:43], vcc
	s_cbranch_execz .LBB0_110
	global_load_dword v28, v[8:9], off
	v_add_f32_e32 v4, v4, v5
	v_add_f32_e32 v2, v2, v3
	v_add_f32_e32 v20, v20, v21
	v_cndmask_b32_e64 v2, v2, v4, s[2:3]
	v_add_f32_e32 v22, v22, v23
	v_cndmask_b32_e64 v2, v2, v20, s[4:5]
	v_add_f32_e32 v18, v18, v24
	v_cndmask_b32_e64 v2, v2, v22, s[6:7]
	v_add_f32_e32 v19, v19, v25
	v_cndmask_b32_e64 v2, v2, v18, s[8:9]
	v_add_f32_e32 v16, v16, v26
	v_cndmask_b32_e64 v2, v2, v19, s[10:11]
	v_add_f32_e32 v17, v17, v27
	v_cndmask_b32_e64 v2, v2, v16, s[12:13]
	s_lshl_b64 s[20:21], s[28:29], 5
	v_cndmask_b32_e64 v2, v2, v17, s[14:15]
	s_waitcnt vmcnt(0)
	v_add_f32_e32 v4, v2, v28
	v_lshl_add_u64 v[2:3], v[10:11], 0, s[20:21]
	global_store_dword v[2:3], v4, off
	s_branch .LBB0_110
